# baseline (speedup 1.0000x reference)
.LBB0_40:
	s_or_b64 exec, exec, s[6:7]
	v_cmp_gt_u32_e32 vcc, 16, v2
	s_and_b64 s[6:7], s[18:19], vcc
	s_and_saveexec_b64 s[4:5], s[6:7]
	v_lshlrev_b32_e32 v2, 2, v2
	v_or_b32_e32 v1, 7, v1
	ds_write_b32 v2, v1
	s_or_b64 exec, exec, s[4:5]
	v_mov_b32_e32 v35, 0
	s_waitcnt lgkmcnt(0)
	s_barrier
	ds_read_b128 v[2:5], v35
	ds_read_b128 v[6:9], v35 offset:16
	ds_read_b128 v[10:13], v35 offset:32
	ds_read_b128 v[14:17], v35 offset:48
	s_and_b64 s[4:5], s[30:31], exec
	s_cselect_b32 s9, s25, s27
	s_cselect_b32 s8, s24, s26
	s_cselect_b32 s11, s21, s23
	s_cselect_b32 s10, s20, s22
	s_lshl_b32 s6, s36, 23
	s_add_u32 s8, s8, s6
	s_addc_u32 s9, s9, 0
	s_or_b32 s6, s34, s33
	s_mulk_i32 s6, 0x880
	s_add_u32 s10, s10, s6
	s_addc_u32 s11, s11, 0
	v_lshlrev_b32_e32 v1, 4, v0
	v_lshlrev_b32_e32 v66, 3, v0
	s_waitcnt lgkmcnt(0)
	v_readfirstlane_b32 s40, v2
	v_readfirstlane_b32 s41, v3
	v_readfirstlane_b32 s42, v4
	v_readfirstlane_b32 s43, v5
	v_readfirstlane_b32 s44, v6
	v_readfirstlane_b32 s45, v7
	v_readfirstlane_b32 s46, v8
	v_readfirstlane_b32 s47, v9
	v_readfirstlane_b32 s48, v10
	v_readfirstlane_b32 s49, v11
	v_readfirstlane_b32 s50, v12
	v_readfirstlane_b32 s51, v13
	v_readfirstlane_b32 s52, v14
	v_readfirstlane_b32 s53, v15
	v_readfirstlane_b32 s54, v16
	v_readfirstlane_b32 s55, v17
	s_max_i32 s12, s40, 0
	s_lshl_b32 s12, s12, 12
	s_add_u32 s12, s8, s12
	s_addc_u32 s13, s9, 0
	global_load_dwordx4 v[2:5], v1, s[12:13] nt
	s_max_i32 s12, s41, 0
	s_lshl_b32 s12, s12, 12
	s_add_u32 s12, s8, s12
	s_addc_u32 s13, s9, 0
	global_load_dwordx4 v[6:9], v1, s[12:13] nt
	s_max_i32 s12, s42, 0
	s_lshl_b32 s12, s12, 12
	s_add_u32 s12, s8, s12
	s_addc_u32 s13, s9, 0
	global_load_dwordx4 v[10:13], v1, s[12:13] nt
	s_max_i32 s12, s43, 0
	s_lshl_b32 s12, s12, 12
	s_add_u32 s12, s8, s12
	s_addc_u32 s13, s9, 0
	global_load_dwordx4 v[14:17], v1, s[12:13] nt
	s_max_i32 s12, s44, 0
	s_lshl_b32 s12, s12, 12
	s_add_u32 s12, s8, s12
	s_addc_u32 s13, s9, 0
	global_load_dwordx4 v[18:21], v1, s[12:13] nt
	s_max_i32 s12, s45, 0
	s_lshl_b32 s12, s12, 12
	s_add_u32 s12, s8, s12
	s_addc_u32 s13, s9, 0
	global_load_dwordx4 v[22:25], v1, s[12:13] nt
	s_max_i32 s12, s46, 0
	s_lshl_b32 s12, s12, 12
	s_add_u32 s12, s8, s12
	s_addc_u32 s13, s9, 0
	global_load_dwordx4 v[26:29], v1, s[12:13] nt
	s_max_i32 s12, s47, 0
	s_lshl_b32 s12, s12, 12
	s_add_u32 s12, s8, s12
	s_addc_u32 s13, s9, 0
	global_load_dwordx4 v[30:33], v1, s[12:13] nt
	s_max_i32 s12, s48, 0
	s_lshl_b32 s12, s12, 12
	s_add_u32 s12, s8, s12
	s_addc_u32 s13, s9, 0
	global_load_dwordx4 v[34:37], v1, s[12:13] nt
	s_max_i32 s12, s49, 0
	s_lshl_b32 s12, s12, 12
	s_add_u32 s12, s8, s12
	s_addc_u32 s13, s9, 0
	global_load_dwordx4 v[38:41], v1, s[12:13] nt
	s_max_i32 s12, s50, 0
	s_lshl_b32 s12, s12, 12
	s_add_u32 s12, s8, s12
	s_addc_u32 s13, s9, 0
	global_load_dwordx4 v[42:45], v1, s[12:13] nt
	s_max_i32 s12, s51, 0
	s_lshl_b32 s12, s12, 12
	s_add_u32 s12, s8, s12
	s_addc_u32 s13, s9, 0
	global_load_dwordx4 v[46:49], v1, s[12:13] nt
	s_max_i32 s12, s52, 0
	s_lshl_b32 s12, s12, 12
	s_add_u32 s12, s8, s12
	s_addc_u32 s13, s9, 0
	global_load_dwordx4 v[50:53], v1, s[12:13] nt
	s_max_i32 s12, s53, 0
	s_lshl_b32 s12, s12, 12
	s_add_u32 s12, s8, s12
	s_addc_u32 s13, s9, 0
	global_load_dwordx4 v[54:57], v1, s[12:13] nt
	s_max_i32 s12, s54, 0
	s_lshl_b32 s12, s12, 12
	s_add_u32 s12, s8, s12
	s_addc_u32 s13, s9, 0
	global_load_dwordx4 v[58:61], v1, s[12:13] nt
	s_max_i32 s12, s55, 0
	s_lshl_b32 s12, s12, 12
	s_add_u32 s12, s8, s12
	s_addc_u32 s13, s9, 0
	global_load_dwordx4 v[62:65], v1, s[12:13] nt
	s_waitcnt vmcnt(14)
	s_cmp_lt_i32 s40, 0
	s_cselect_b32 s14, 0, -1
	v_cvt_pk_f16_f32 v2, v2, v3
	v_cvt_pk_f16_f32 v3, v4, v5
	v_and_b32_e32 v2, s14, v2
	v_and_b32_e32 v3, s14, v3
	global_store_dwordx2 v66, v[2:3], s[10:11]
	s_cmp_lt_i32 s41, 0
	s_cselect_b32 s14, 0, -1
	v_cvt_pk_f16_f32 v6, v6, v7
	v_cvt_pk_f16_f32 v7, v8, v9
	v_and_b32_e32 v6, s14, v6
	v_and_b32_e32 v7, s14, v7
	global_store_dwordx2 v66, v[6:7], s[10:11] offset:2176
	s_add_u32 s10, s10, 0x1100
	s_addc_u32 s11, s11, 0
	s_waitcnt vmcnt(14)
	s_cmp_lt_i32 s42, 0
	s_cselect_b32 s14, 0, -1
	v_cvt_pk_f16_f32 v10, v10, v11
	v_cvt_pk_f16_f32 v11, v12, v13
	v_and_b32_e32 v10, s14, v10
	v_and_b32_e32 v11, s14, v11
	global_store_dwordx2 v66, v[10:11], s[10:11]
	s_cmp_lt_i32 s43, 0
	s_cselect_b32 s14, 0, -1
	v_cvt_pk_f16_f32 v14, v14, v15
	v_cvt_pk_f16_f32 v15, v16, v17
	v_and_b32_e32 v14, s14, v14
	v_and_b32_e32 v15, s14, v15
	global_store_dwordx2 v66, v[14:15], s[10:11] offset:2176
	s_add_u32 s10, s10, 0x1100
	s_addc_u32 s11, s11, 0
	s_waitcnt vmcnt(14)
	s_cmp_lt_i32 s44, 0
	s_cselect_b32 s14, 0, -1
	v_cvt_pk_f16_f32 v18, v18, v19
	v_cvt_pk_f16_f32 v19, v20, v21
	v_and_b32_e32 v18, s14, v18
	v_and_b32_e32 v19, s14, v19
	global_store_dwordx2 v66, v[18:19], s[10:11]
	s_cmp_lt_i32 s45, 0
	s_cselect_b32 s14, 0, -1
	v_cvt_pk_f16_f32 v22, v22, v23
	v_cvt_pk_f16_f32 v23, v24, v25
	v_and_b32_e32 v22, s14, v22
	v_and_b32_e32 v23, s14, v23
	global_store_dwordx2 v66, v[22:23], s[10:11] offset:2176
	s_add_u32 s10, s10, 0x1100
	s_addc_u32 s11, s11, 0
	s_waitcnt vmcnt(14)
	s_cmp_lt_i32 s46, 0
	s_cselect_b32 s14, 0, -1
	v_cvt_pk_f16_f32 v26, v26, v27
	v_cvt_pk_f16_f32 v27, v28, v29
	v_and_b32_e32 v26, s14, v26
	v_and_b32_e32 v27, s14, v27
	global_store_dwordx2 v66, v[26:27], s[10:11]
	s_cmp_lt_i32 s47, 0
	s_cselect_b32 s14, 0, -1
	v_cvt_pk_f16_f32 v30, v30, v31
	v_cvt_pk_f16_f32 v31, v32, v33
	v_and_b32_e32 v30, s14, v30
	v_and_b32_e32 v31, s14, v31
	global_store_dwordx2 v66, v[30:31], s[10:11] offset:2176
	s_add_u32 s10, s10, 0x1100
	s_addc_u32 s11, s11, 0
	s_waitcnt vmcnt(14)
	s_cmp_lt_i32 s48, 0
	s_cselect_b32 s14, 0, -1
	v_cvt_pk_f16_f32 v34, v34, v35
	v_cvt_pk_f16_f32 v35, v36, v37
	v_and_b32_e32 v34, s14, v34
	v_and_b32_e32 v35, s14, v35
	global_store_dwordx2 v66, v[34:35], s[10:11]
	s_cmp_lt_i32 s49, 0
	s_cselect_b32 s14, 0, -1
	v_cvt_pk_f16_f32 v38, v38, v39
	v_cvt_pk_f16_f32 v39, v40, v41
	v_and_b32_e32 v38, s14, v38
	v_and_b32_e32 v39, s14, v39
	global_store_dwordx2 v66, v[38:39], s[10:11] offset:2176
	s_add_u32 s10, s10, 0x1100
	s_addc_u32 s11, s11, 0
	s_waitcnt vmcnt(14)
	s_cmp_lt_i32 s50, 0
	s_cselect_b32 s14, 0, -1
	v_cvt_pk_f16_f32 v42, v42, v43
	v_cvt_pk_f16_f32 v43, v44, v45
	v_and_b32_e32 v42, s14, v42
	v_and_b32_e32 v43, s14, v43
	global_store_dwordx2 v66, v[42:43], s[10:11]
	s_cmp_lt_i32 s51, 0
	s_cselect_b32 s14, 0, -1
	v_cvt_pk_f16_f32 v46, v46, v47
	v_cvt_pk_f16_f32 v47, v48, v49
	v_and_b32_e32 v46, s14, v46
	v_and_b32_e32 v47, s14, v47
	global_store_dwordx2 v66, v[46:47], s[10:11] offset:2176
	s_add_u32 s10, s10, 0x1100
	s_addc_u32 s11, s11, 0
	s_waitcnt vmcnt(14)
	s_cmp_lt_i32 s52, 0
	s_cselect_b32 s14, 0, -1
	v_cvt_pk_f16_f32 v50, v50, v51
	v_cvt_pk_f16_f32 v51, v52, v53
	v_and_b32_e32 v50, s14, v50
	v_and_b32_e32 v51, s14, v51
	global_store_dwordx2 v66, v[50:51], s[10:11]
	s_cmp_lt_i32 s53, 0
	s_cselect_b32 s14, 0, -1
	v_cvt_pk_f16_f32 v54, v54, v55
	v_cvt_pk_f16_f32 v55, v56, v57
	v_and_b32_e32 v54, s14, v54
	v_and_b32_e32 v55, s14, v55
	global_store_dwordx2 v66, v[54:55], s[10:11] offset:2176
	s_add_u32 s10, s10, 0x1100
	s_addc_u32 s11, s11, 0
	s_waitcnt vmcnt(14)
	s_cmp_lt_i32 s54, 0
	s_cselect_b32 s14, 0, -1
	v_cvt_pk_f16_f32 v58, v58, v59
	v_cvt_pk_f16_f32 v59, v60, v61
	v_and_b32_e32 v58, s14, v58
	v_and_b32_e32 v59, s14, v59
	global_store_dwordx2 v66, v[58:59], s[10:11]
	s_cmp_lt_i32 s55, 0
	s_cselect_b32 s14, 0, -1
	v_cvt_pk_f16_f32 v62, v62, v63
	v_cvt_pk_f16_f32 v63, v64, v65
	v_and_b32_e32 v62, s14, v62
	v_and_b32_e32 v63, s14, v63
	global_store_dwordx2 v66, v[62:63], s[10:11] offset:2176
	s_endpgm

	.amdhsa_kernel _Z11prep_kernelPKfS0_S0_PKiS0_S0_S0_S0_PDF16_S3_S3_S3_Pi
		.amdhsa_group_segment_fixed_size 80
		.amdhsa_private_segment_fixed_size 0
		.amdhsa_kernarg_size 104
		.amdhsa_user_sgpr_count 2
		.amdhsa_user_sgpr_dispatch_ptr 0
		.amdhsa_user_sgpr_queue_ptr 0
		.amdhsa_user_sgpr_kernarg_segment_ptr 1
		.amdhsa_user_sgpr_dispatch_id 0
		.amdhsa_user_sgpr_kernarg_preload_length 0
		.amdhsa_user_sgpr_kernarg_preload_offset 0
		.amdhsa_user_sgpr_private_segment_size 0
		.amdhsa_uses_dynamic_stack 0
		.amdhsa_enable_private_segment 0
		.amdhsa_system_sgpr_workgroup_id_x 1
		.amdhsa_system_sgpr_workgroup_id_y 0
		.amdhsa_system_sgpr_workgroup_id_z 0
		.amdhsa_system_sgpr_workgroup_info 0
		.amdhsa_system_vgpr_workitem_id 0
		.amdhsa_next_free_vgpr 72
		.amdhsa_next_free_sgpr 56
		.amdhsa_accum_offset 72
		.amdhsa_reserve_vcc 1
		.amdhsa_float_round_mode_32 0
		.amdhsa_float_round_mode_16_64 0
		.amdhsa_float_denorm_mode_32 3
		.amdhsa_float_denorm_mode_16_64 3
		.amdhsa_dx10_clamp 1
		.amdhsa_ieee_mode 1
		.amdhsa_fp16_overflow 0
		.amdhsa_tg_split 0
		.amdhsa_exception_fp_ieee_invalid_op 0
		.amdhsa_exception_fp_denorm_src 0
		.amdhsa_exception_fp_ieee_div_zero 0
		.amdhsa_exception_fp_ieee_overflow 0
		.amdhsa_exception_fp_ieee_underflow 0
		.amdhsa_exception_fp_ieee_inexact 0
		.amdhsa_exception_int_div_zero 0
	.end_amdhsa_kernel

amdhsa.kernels:
  - .agpr_count:     0
    .args:
      - .actual_access:  read_only
        .address_space:  global
        .offset:         0
        .size:           8
        .value_kind:     global_buffer
      - .actual_access:  read_only
        .address_space:  global
        .offset:         8
        .size:           8
        .value_kind:     global_buffer
      - .actual_access:  read_only
        .address_space:  global
        .offset:         16
        .size:           8
        .value_kind:     global_buffer
      - .actual_access:  read_only
        .address_space:  global
        .offset:         24
        .size:           8
        .value_kind:     global_buffer
      - .actual_access:  read_only
        .address_space:  global
        .offset:         32
        .size:           8
        .value_kind:     global_buffer
      - .actual_access:  read_only
        .address_space:  global
        .offset:         40
        .size:           8
        .value_kind:     global_buffer
      - .actual_access:  read_only
        .address_space:  global
        .offset:         48
        .size:           8
        .value_kind:     global_buffer
      - .actual_access:  read_only
        .address_space:  global
        .offset:         56
        .size:           8
        .value_kind:     global_buffer
      - .actual_access:  write_only
        .address_space:  global
        .offset:         64
        .size:           8
        .value_kind:     global_buffer
      - .actual_access:  write_only
        .address_space:  global
        .offset:         72
        .size:           8
        .value_kind:     global_buffer
      - .actual_access:  write_only
        .address_space:  global
        .offset:         80
        .size:           8
        .value_kind:     global_buffer
      - .actual_access:  write_only
        .address_space:  global
        .offset:         88
        .size:           8
        .value_kind:     global_buffer
      - .actual_access:  write_only
        .address_space:  global
        .offset:         96
        .size:           8
        .value_kind:     global_buffer
    .group_segment_fixed_size: 80
    .kernarg_segment_align: 8
    .kernarg_segment_size: 104
    .language:       OpenCL C
    .language_version:
      - 2
      - 0
    .max_flat_workgroup_size: 256
    .name:           _Z11prep_kernelPKfS0_S0_PKiS0_S0_S0_S0_PDF16_S3_S3_S3_Pi
    .private_segment_fixed_size: 0
    .sgpr_count:     62
    .sgpr_spill_count: 0
    .symbol:         _Z11prep_kernelPKfS0_S0_PKiS0_S0_S0_S0_PDF16_S3_S3_S3_Pi.kd
    .uniform_work_group_size: 1
    .uses_dynamic_stack: false
    .vgpr_count:     72
    .vgpr_spill_count: 0
    .wavefront_size: 64
  - .agpr_count:     0
    .args:
      - .address_space:  global
        .offset:         0
        .size:           8
        .value_kind:     global_buffer
      - .address_space:  global
        .offset:         8
        .size:           8
        .value_kind:     global_buffer
      - .address_space:  global
        .offset:         16
        .size:           8
        .value_kind:     global_buffer
      - .address_space:  global
        .offset:         24
        .size:           8
        .value_kind:     global_buffer
      - .actual_access:  read_only
        .address_space:  global
        .offset:         32
        .size:           8
        .value_kind:     global_buffer
      - .actual_access:  read_only
        .address_space:  global
        .offset:         40
        .size:           8
        .value_kind:     global_buffer
      - .actual_access:  read_only
        .address_space:  global
        .offset:         48
        .size:           8
        .value_kind:     global_buffer
      - .actual_access:  read_only
        .address_space:  global
        .offset:         56
        .size:           8
        .value_kind:     global_buffer
      - .actual_access:  read_only
        .address_space:  global
        .offset:         64
        .size:           8
        .value_kind:     global_buffer
      - .actual_access:  read_only
        .address_space:  global
        .offset:         72
        .size:           8
        .value_kind:     global_buffer
      - .actual_access:  write_only
        .address_space:  global
        .offset:         80
        .size:           8
        .value_kind:     global_buffer
      - .actual_access:  write_only
        .address_space:  global
        .offset:         88
        .size:           8
        .value_kind:     global_buffer
      - .actual_access:  write_only
        .address_space:  global
        .offset:         96
        .size:           8
        .value_kind:     global_buffer
    .group_segment_fixed_size: 28672
    .kernarg_segment_align: 8
    .kernarg_segment_size: 104
    .language:       OpenCL C
    .language_version:
      - 2
      - 0
    .max_flat_workgroup_size: 512
    .name:           _Z11proj_kernelPKDF16_S0_S0_S0_PKiPKfS4_S4_S4_S4_PDF16_S5_S5_
    .private_segment_fixed_size: 0
    .sgpr_count:     66
    .sgpr_spill_count: 0
    .symbol:         _Z11proj_kernelPKDF16_S0_S0_S0_PKiPKfS4_S4_S4_S4_PDF16_S5_S5_.kd
    .uniform_work_group_size: 1
    .uses_dynamic_stack: false
    .vgpr_count:     217
    .vgpr_spill_count: 0
    .wavefront_size: 64
  - .agpr_count:     0
    .args:
      - .actual_access:  read_only
        .address_space:  global
        .offset:         0
        .size:           8
        .value_kind:     global_buffer
      - .address_space:  global
        .offset:         8
        .size:           8
        .value_kind:     global_buffer
      - .address_space:  global
        .offset:         16
        .size:           8
        .value_kind:     global_buffer
      - .actual_access:  read_only
        .address_space:  global
        .offset:         24
        .size:           8
        .value_kind:     global_buffer
      - .actual_access:  write_only
        .address_space:  global
        .offset:         32
        .size:           8
        .value_kind:     global_buffer
      - .actual_access:  read_only
        .address_space:  global
        .offset:         40
        .size:           8
        .value_kind:     global_buffer
      - .actual_access:  write_only
        .address_space:  global
        .offset:         48
        .size:           8
        .value_kind:     global_buffer
    .group_segment_fixed_size: 0
    .kernarg_segment_align: 8
    .kernarg_segment_size: 56
    .language:       OpenCL C
    .language_version:
      - 2
      - 0
    .max_flat_workgroup_size: 512
    .name:           _Z11attn_kernelPKDF16_S0_S0_PKiPDF16_PKfS3_
    .private_segment_fixed_size: 0
    .sgpr_count:     100
    .sgpr_spill_count: 0
    .symbol:         _Z11attn_kernelPKDF16_S0_S0_PKiPDF16_PKfS3_.kd
    .uniform_work_group_size: 1
    .uses_dynamic_stack: false
    .vgpr_count:     204
    .vgpr_spill_count: 0
    .wavefront_size: 64
  - .agpr_count:     0
    .args:
      - .address_space:  global
        .offset:         0
        .size:           8
        .value_kind:     global_buffer
      - .address_space:  global
        .offset:         8
        .size:           8
        .value_kind:     global_buffer
      - .actual_access:  read_only
        .address_space:  global
        .offset:         16
        .size:           8
        .value_kind:     global_buffer
      - .actual_access:  write_only
        .address_space:  global
        .offset:         24
        .size:           8
        .value_kind:     global_buffer
    .group_segment_fixed_size: 0
    .kernarg_segment_align: 8
    .kernarg_segment_size: 32
    .language:       OpenCL C
    .language_version:
      - 2
      - 0
    .max_flat_workgroup_size: 512
    .name:           _Z12oproj_kernelPKDF16_S0_PKfPf
    .private_segment_fixed_size: 0
    .sgpr_count:     33
    .sgpr_spill_count: 0
    .symbol:         _Z12oproj_kernelPKDF16_S0_PKfPf.kd
    .uniform_work_group_size: 1
    .uses_dynamic_stack: false
    .vgpr_count:     108
    .vgpr_spill_count: 0
    .wavefront_size: 64
